# mixer phase: one static s_setprio 1 for waves 0-3 across the attention/pool units (reset to 0 at phase end)
# speedup vs baseline: 1.0026x; 1.0026x over previous
.LBB0_526:
	s_andn2_b64 vcc, exec, s[26:27]
	s_cbranch_vccnz .LBB0_624
	s_load_dwordx2 s[52:53], s[0:1], 0x98
	v_readlane_b32 s4, v254, 32
	s_cmp_ge_u32 s4, 4
	s_cbranch_scc1 .Lpm_skip
	s_setprio 1
.Lpm_skip:
	s_add_i32 s4, s89, 6
	s_and_b32 s5, s72, 3
	s_cmp_lt_u32 s4, 15
	s_cselect_b32 s54, s5, -1
	s_cmp_lg_u32 s54, 0
	s_cbranch_scc1 .LBB0_540
	s_cmpk_gt_i32 s72, 0x3ff
	s_waitcnt lgkmcnt(0)
	s_barrier
	s_cbranch_scc1 .LBB0_539
	s_load_dwordx2 s[26:27], s[0:1], 0x68
	s_add_i32 s16, s72, 0x400
	s_ashr_i32 s36, s16, 6
	s_ashr_i32 s37, s36, 31
	s_lshl_b64 s[4:5], s[36:37], 23
	s_waitcnt lgkmcnt(0)
	s_add_u32 s30, s26, s4
	s_addc_u32 s31, s27, s5
	s_add_u32 s5, s52, 0x2000000
	s_addc_u32 s14, s53, 0
	s_lshl_b64 s[36:37], s[36:37], 21
	s_add_u32 s36, s5, s36
	s_addc_u32 s37, s14, s37
	s_lshl_b32 s17, s72, 4
	s_and_b32 s4, s17, 0x380
	s_lshl_b32 s6, s72, 8
	s_add_i32 s94, s4, s29
	s_and_b32 s15, s6, 0x700
	s_lshl_b64 s[38:39], s[94:95], 13
	s_add_u32 s38, s30, s38
	s_waitcnt vmcnt(0)
	v_lshlrev_b32_e32 v2, 2, v194
	s_addc_u32 s39, s31, s39
	s_lshl_b32 s40, s15, 2
	v_ashrrev_i32_e32 v3, 31, v2
	s_add_u32 s38, s38, s40
	s_addc_u32 s39, s39, 0
	v_lshlrev_b64 v[130:131], 2, v[2:3]
	v_lshl_add_u64 v[2:3], s[38:39], 0, v[130:131]
	s_or_b32 s38, s94, 1
	s_mov_b32 s39, s95
	s_lshl_b64 s[38:39], s[38:39], 13
	s_add_u32 s38, s30, s38
	s_addc_u32 s39, s31, s39
	s_add_u32 s38, s38, s40
	s_addc_u32 s39, s39, 0
	s_waitcnt vmcnt(14)
	v_lshl_add_u64 v[6:7], s[38:39], 0, v[130:131]
	s_or_b32 s38, s94, 2
	s_mov_b32 s39, s95
	s_lshl_b64 s[38:39], s[38:39], 13
	s_add_u32 s38, s30, s38
	s_addc_u32 s39, s31, s39
	s_add_u32 s38, s38, s40
	s_addc_u32 s39, s39, 0
	s_waitcnt vmcnt(13)
	v_lshl_add_u64 v[10:11], s[38:39], 0, v[130:131]
	s_or_b32 s38, s94, 3
	s_mov_b32 s39, s95
	s_lshl_b64 s[38:39], s[38:39], 13
	s_add_u32 s38, s30, s38
	s_addc_u32 s39, s31, s39
	s_add_u32 s38, s38, s40
	s_addc_u32 s39, s39, 0
	s_waitcnt vmcnt(12)
	v_lshl_add_u64 v[14:15], s[38:39], 0, v[130:131]
	s_or_b32 s38, s94, 4
	s_mov_b32 s39, s95
	s_lshl_b64 s[38:39], s[38:39], 13
	s_add_u32 s38, s30, s38
	s_addc_u32 s39, s31, s39
	s_add_u32 s38, s38, s40
	s_addc_u32 s39, s39, 0
	s_waitcnt vmcnt(11)
	v_lshl_add_u64 v[18:19], s[38:39], 0, v[130:131]
	s_or_b32 s38, s94, 5
	s_mov_b32 s39, s95
	s_lshl_b64 s[38:39], s[38:39], 13
	s_add_u32 s38, s30, s38
	s_addc_u32 s39, s31, s39
	s_add_u32 s38, s38, s40
	s_addc_u32 s39, s39, 0
	s_waitcnt vmcnt(10)
	v_lshl_add_u64 v[22:23], s[38:39], 0, v[130:131]
	s_or_b32 s38, s94, 6
	s_mov_b32 s39, s95
	s_lshl_b64 s[38:39], s[38:39], 13
	s_add_u32 s38, s30, s38
	s_addc_u32 s39, s31, s39
	s_add_u32 s38, s38, s40
	s_addc_u32 s39, s39, 0
	s_waitcnt vmcnt(9)
	v_lshl_add_u64 v[26:27], s[38:39], 0, v[130:131]
	s_or_b32 s38, s94, 7
	s_mov_b32 s39, s95
	s_lshl_b64 s[38:39], s[38:39], 13
	s_add_u32 s38, s30, s38
	s_addc_u32 s39, s31, s39
	s_add_u32 s38, s38, s40
	s_addc_u32 s39, s39, 0
	s_waitcnt vmcnt(8)
	v_lshl_add_u64 v[30:31], s[38:39], 0, v[130:131]
	s_add_i32 s38, s94, 64
	s_mov_b32 s39, s95
	s_lshl_b64 s[38:39], s[38:39], 13
	s_add_u32 s38, s30, s38
	s_addc_u32 s39, s31, s39
	s_add_u32 s38, s38, s40
	s_addc_u32 s39, s39, 0
	s_waitcnt vmcnt(7)
	v_lshl_add_u64 v[34:35], s[38:39], 0, v[130:131]
	s_add_i32 s38, s94, 0x41
	s_mov_b32 s39, s95
	s_lshl_b64 s[38:39], s[38:39], 13
	s_add_u32 s38, s30, s38
	s_addc_u32 s39, s31, s39
	s_add_u32 s38, s38, s40
	s_addc_u32 s39, s39, 0
	s_waitcnt vmcnt(6)
	v_lshl_add_u64 v[38:39], s[38:39], 0, v[130:131]
	s_add_i32 s38, s94, 0x42
	s_mov_b32 s39, s95
	s_lshl_b64 s[38:39], s[38:39], 13
	s_add_u32 s38, s30, s38
	s_addc_u32 s39, s31, s39
	s_add_u32 s38, s38, s40
	s_addc_u32 s39, s39, 0
	s_waitcnt vmcnt(5)
	v_lshl_add_u64 v[42:43], s[38:39], 0, v[130:131]
	s_add_i32 s38, s94, 0x43
	s_mov_b32 s39, s95
	s_lshl_b64 s[38:39], s[38:39], 13
	s_add_u32 s38, s30, s38
	s_addc_u32 s39, s31, s39
	s_add_u32 s38, s38, s40
	s_addc_u32 s39, s39, 0
	v_lshl_add_u64 v[44:45], s[38:39], 0, v[130:131]
	s_add_i32 s38, s94, 0x44
	s_mov_b32 s39, s95
	s_lshl_b64 s[38:39], s[38:39], 13
	s_add_u32 s38, s30, s38
	s_addc_u32 s39, s31, s39
	s_add_u32 s38, s38, s40
	s_addc_u32 s39, s39, 0
	global_load_dwordx4 v[2:5], v[2:3], off nt
	s_nop 0
	global_load_dwordx4 v[6:9], v[6:7], off nt
	s_nop 0
	global_load_dwordx4 v[10:13], v[10:11], off nt
	s_nop 0
	global_load_dwordx4 v[14:17], v[14:15], off nt
	s_nop 0
	global_load_dwordx4 v[18:21], v[18:19], off nt
	s_nop 0
	global_load_dwordx4 v[22:25], v[22:23], off nt
	s_nop 0
	global_load_dwordx4 v[26:29], v[26:27], off nt
	s_nop 0
	global_load_dwordx4 v[30:33], v[30:31], off nt
	s_nop 0
	global_load_dwordx4 v[34:37], v[34:35], off nt
	s_nop 0
	global_load_dwordx4 v[38:41], v[38:39], off nt
	s_nop 0
	global_load_dwordx4 v[50:53], v[42:43], off nt
	global_load_dwordx4 v[54:57], v[44:45], off nt
	v_lshl_add_u64 v[42:43], s[38:39], 0, v[130:131]
	s_add_i32 s38, s94, 0x45
	s_mov_b32 s39, s95
	s_lshl_b64 s[38:39], s[38:39], 13
	s_add_u32 s38, s30, s38
	s_addc_u32 s39, s31, s39
	s_add_u32 s38, s38, s40
	s_addc_u32 s39, s39, 0
	v_lshl_add_u64 v[44:45], s[38:39], 0, v[130:131]
	s_add_i32 s38, s94, 0x46
	s_mov_b32 s39, s95
	s_lshl_b64 s[38:39], s[38:39], 13
	s_add_u32 s38, s30, s38
	s_addc_u32 s39, s31, s39
	s_add_u32 s38, s38, s40
	s_addc_u32 s39, s39, 0
	s_addk_i32 s94, 0x47
	global_load_dwordx4 v[74:77], v[42:43], off nt
	global_load_dwordx4 v[78:81], v[44:45], off nt
	v_lshl_add_u64 v[42:43], s[38:39], 0, v[130:131]
	s_lshl_b64 s[38:39], s[94:95], 13
	s_add_u32 s30, s30, s38
	s_addc_u32 s31, s31, s39
	s_add_u32 s30, s30, s40
	s_addc_u32 s31, s31, 0
	v_lshl_add_u64 v[44:45], s[30:31], 0, v[130:131]
	global_load_dwordx4 v[98:101], v[42:43], off nt
	global_load_dwordx4 v[102:105], v[44:45], off nt
	v_readlane_b32 s30, v254, 32
	s_waitcnt vmcnt(20)
	v_add_u32_e32 v47, 0x200, v192
	v_add_u32_e32 v48, 0x400, v192
	v_bitop3_b32 v0, v194, s30, 15 bitop3:0x6c
	v_readlane_b32 s30, v253, 15
	v_lshlrev_b32_e32 v43, 3, v0
	v_add_u32_e32 v49, 0x600, v192
	v_bitop3_b32 v0, v194, s30, 15 bitop3:0x6c
	v_lshlrev_b32_e32 v44, 3, v0
	v_lshrrev_b32_e32 v0, 6, v192
	v_xor_b32_e32 v0, v0, v194
	v_lshlrev_b32_e32 v0, 4, v0
	v_and_b32_e32 v0, 0x70, v0
	v_add_u32_e32 v45, 0, v0
	v_and_b32_e32 v0, 32, v194
	v_ashrrev_i32_e32 v132, 3, v192
	v_ashrrev_i32_e32 v134, 3, v47
	v_ashrrev_i32_e32 v136, 3, v48
	v_ashrrev_i32_e32 v138, 3, v49
	v_lshl_add_u32 v42, v194, 9, 0
	v_cmp_eq_u32_e64 s[38:39], 0, v0
	v_lshlrev_b32_e32 v0, 4, v194
	v_lshlrev_b32_e32 v46, 7, v132
	v_lshlrev_b32_e32 v47, 7, v134
	v_lshlrev_b32_e32 v48, 7, v136
	v_lshlrev_b32_e32 v49, 7, v138
	v_and_b32_e32 v0, 0x70, v0
	v_and_b32_e32 v133, 0x7f, v132
	v_and_b32_e32 v135, 0x7f, v134
	v_and_b32_e32 v137, 0x7f, v136
	v_and_b32_e32 v139, 0x7f, v138
	s_add_i32 s43, s6, 0x40000
	s_add_i32 s48, s17, 0x4000
	v_add_u32_e32 v140, v42, v43
	v_add_u32_e32 v141, v42, v44
	v_add_u32_e32 v142, v45, v46
	v_add_u32_e32 v143, v45, v47
	v_add_u32_e32 v144, v45, v48
	v_add_u32_e32 v145, v45, v49
	s_mov_b32 s94, s4
	v_readlane_b32 s31, v254, 33
	s_branch .LBB0_532

.LBB0_1063:
	s_setprio 0
	v_readlane_b32 s4, v253, 1
	s_add_i32 s34, s34, 1
	v_readlane_b32 s5, v253, 2
	s_cmp_ge_i32 s34, s5
	s_mov_b64 s[4:5], -1
	s_cbranch_scc0 .LBB0_1064
	s_getpc_b64 s[98:99]
